# baseline (speedup 1.0000x reference)
_Z11mega_kernelPKfPDF16_PKDF16_S3_S1_PfS0_S0_PK15HIP_vector_typeIfLj2EEPS6_:
	s_load_dwordx4 s[4:7], s[0:1], 0x40
	s_getreg_b32 s2, hwreg(HW_REG_XCC_ID, 0, 4)
	s_load_dwordx8 s[36:43], s[0:1], 0x0
	s_load_dwordx8 s[44:51], s[0:1], 0x20
	s_mov_b64 s[56:57], src_shared_base
	s_mov_b32 s59, 0
	s_waitcnt lgkmcnt(0)
	s_add_u32 s60, s6, 0x60000
	s_addc_u32 s61, s7, 0
	s_add_u32 s96, s6, 0x60200
	s_addc_u32 s97, s7, 0
	s_add_u32 s64, s6, 0x60400
	s_addc_u32 s65, s7, 0
	s_add_u32 s8, s6, 0x60c00
	s_addc_u32 s9, s7, 0
	v_writelane_b32 v230, s8, 0
	s_lshl_b32 s2, s2, 7
	s_and_b32 s2, s2, 0x380
	v_writelane_b32 v230, s9, 1
	s_add_u32 s2, s6, s2
	v_writelane_b32 v230, s4, 2
	s_addc_u32 s3, s7, 0
	s_add_u32 s68, s2, 0x60800
	v_writelane_b32 v230, s5, 3
	v_writelane_b32 v230, s6, 4
	v_writelane_b32 v230, s7, 5
	s_addc_u32 s69, s3, 0
	s_add_i32 s2, 0, 0x10000
	v_writelane_b32 v230, s2, 6
	s_add_i32 s2, 0, 0x14000
	v_writelane_b32 v230, s2, 7
	s_add_i32 s2, 0, 0x18000
	v_writelane_b32 v230, s2, 8
	s_add_i32 s2, 0, 0x1c000
	v_cmp_eq_u32_e64 s[34:35], 0, v0
	v_mov_b32_e32 v106, -1
	v_mov_b32_e32 v231, -1
	s_mov_b64 s[70:71], 0
	v_mov_b32_e32 v109, 0
	v_mov_b32_e32 v1, 1
	s_movk_i32 s56, 0x600
	s_mov_b32 s33, 0x10000
	s_movk_i32 s63, 0x2000
	s_mov_b32 s90, 0x14000
	s_movk_i32 s74, 0x4000
	s_movk_i32 s75, 0x6000
	s_mov_b32 s53, 0x8000
	s_mov_b32 s54, 0xa000
	v_writelane_b32 v230, s2, 9
	s_mov_b32 s55, 0xc000
	s_mov_b32 s66, 0xe000
	s_movk_i32 s67, 0x300
	s_movk_i32 s62, 0xc00
	s_add_i32 s2, 0, 0x1200
	s_mov_b32 s91, 0x12000
	s_mov_b32 s52, 0x16000
	v_mov_b32_e32 v168, 0x64
	v_mov_b32_e32 v169, 0xc0
	v_mov_b32_e32 v170, 48
	v_mov_b32_e32 v171, 2
	v_mov_b32_e32 v172, 0xffffff80
	v_mov_b32_e32 v173, -1
	s_mov_b64 s[78:79], 0x30080
	s_mov_b64 s[80:81], 0x100
	s_mov_b64 s[82:83], 0x24100
	s_mov_b64 s[84:85], 0x30100
	s_mov_b64 s[86:87], 0x180
	s_mov_b64 s[88:89], 0x24180
	v_writelane_b32 v230, s2, 10
	s_branch .LBB1_4

.LBB1_4:
	s_and_saveexec_b64 s[0:1], s[34:35]
	s_cbranch_execz .LBB1_30
	v_mov_b32_e32 v2, -1
	v_cmp_lt_i32_e32 vcc, -1, v173
	v_mov_b32_e32 v3, 0
	s_and_saveexec_b64 s[2:3], vcc
	s_cbranch_execz .LBB1_7
	v_readfirstlane_b32 s4, v231
	s_cmp_lt_i32 s4, 0
	s_cbranch_scc1 .Lq_nopf
	v_mov_b32_e32 v2, v231
	v_mov_b32_e32 v231, -1
	s_branch .Lq_join
.Lq_nopf:
	v_lshlrev_b32_e32 v108, 5, v173
	v_lshl_add_u64 v[2:3], v[108:109], 2, s[64:65]
	global_atomic_add v2, v[2:3], v1, off sc0
	s_waitcnt vmcnt(0)
.Lq_join:
	s_movk_i32 s4, 0x90
	v_cmp_gt_i32_e32 vcc, s4, v2
	s_nop 1
	v_cndmask_b32_e32 v3, 0, v173, vcc
	v_cndmask_b32_e32 v2, -1, v2, vcc

.LBB1_30:
	s_or_b64 exec, exec, s[0:1]
	s_waitcnt lgkmcnt(0)
	s_barrier
	ds_read_b64 v[2:3], v109
	s_mov_b64 s[0:1], -1
	s_waitcnt lgkmcnt(0)
	s_barrier
	v_cmp_lt_i32_e32 vcc, -1, v2
	s_and_saveexec_b64 s[92:93], vcc
	s_cbranch_execz .LBB1_3
	v_and_b32_e32 v4, 0x7fffffe1, v2
	v_cmp_ne_u32_e32 vcc, 1, v4
	s_and_saveexec_b64 s[0:1], vcc
	s_xor_b64 s[0:1], exec, s[0:1]
	v_writelane_b32 v230, s0, 11
	s_nop 1
	v_writelane_b32 v230, s1, 12
	s_cbranch_execz .LBB1_212
	v_cmp_gt_u32_e32 vcc, 32, v2
	s_and_saveexec_b64 s[0:1], vcc
	s_xor_b64 s[0:1], exec, s[0:1]
	v_lshrrev_b32_e32 v4, 3, v2
	v_lshrrev_b32_e32 v2, 1, v2
	s_or_saveexec_b64 s[0:1], s[0:1]
	s_mov_b64 s[2:3], -1
	s_xor_b64 exec, exec, s[0:1]
	s_cbranch_execz .LBB1_44
	v_cmp_lt_u32_e32 vcc, 63, v2
	s_and_saveexec_b64 s[2:3], vcc
	s_xor_b64 s[2:3], exec, s[2:3]
	s_cbranch_execz .LBB1_41
	s_movk_i32 s4, 0x5f
	v_cmp_lt_u32_e32 vcc, s4, v2
	s_and_saveexec_b64 s[4:5], vcc
	s_xor_b64 s[4:5], exec, s[4:5]
	v_add_u32_e32 v4, 0xffffffa0, v2
	v_lshrrev_b32_e32 v4, 2, v4
	v_add_u32_e32 v4, 4, v4
	s_or_saveexec_b64 s[6:7], s[4:5]
	s_mov_b64 s[4:5], 0
	s_xor_b64 exec, exec, s[6:7]
	v_subrev_u32_e32 v4, 64, v2
	v_and_b32_e32 v5, 4, v2
	v_lshrrev_b32_e32 v4, 3, v4
	v_add_u32_e32 v6, 12, v4
	v_cmp_eq_u32_e32 vcc, 0, v5
	s_and_b64 s[4:5], vcc, exec
	s_nop 0
	v_cndmask_b32_e32 v4, v4, v6, vcc
	s_or_b64 exec, exec, s[6:7]

.LBB1_52:
	ds_read_b128 v[138:141], v135
	ds_read_b128 v[142:145], v135 offset:1024
	ds_read_b128 v[146:149], v135 offset:2048
	ds_read_b128 v[150:153], v135 offset:3072
	ds_read_b128 v[154:157], v135 offset:4096
	ds_read_b128 v[158:161], v135 offset:5120
	v_add_u32_e32 v136, 0xc000, v120
	v_lshl_add_u64 v[166:167], v[110:111], 0, s[2:3]
	v_readfirstlane_b32 s5, v136
	v_add_u32_e32 v137, 0xe000, v120
	v_lshl_add_u64 v[194:195], v[166:167], 0, s[78:79]
	s_mov_b32 m0, s5
	v_lshl_add_u64 v[218:219], v[112:113], 0, s[2:3]
	v_readfirstlane_b32 s5, v137
	ds_read_b128 v[162:165], v121
	ds_read_b128 v[182:185], v121 offset:1024
	ds_read_b128 v[186:189], v108
	ds_read_b128 v[190:193], v108 offset:1024
	global_load_lds_dwordx4 v[194:195], off
	v_lshl_add_u64 v[194:195], v[218:219], 0, s[78:79]
	s_mov_b32 m0, s5
	s_nop 0
	global_load_lds_dwordx4 v[194:195], off
	s_waitcnt lgkmcnt(4)
	s_barrier
	s_waitcnt lgkmcnt(0)
	s_setprio 1
	s_waitcnt lgkmcnt(0)
	v_mfma_f32_16x16x32_f16 v[94:97], v[162:165], v[138:141], v[94:97]
	v_mfma_f32_16x16x32_f16 v[90:93], v[162:165], v[146:149], v[90:93]
	v_mfma_f32_16x16x32_f16 v[86:89], v[162:165], v[154:157], v[86:89]
	v_mfma_f32_16x16x32_f16 v[82:85], v[186:189], v[138:141], v[82:85]
	v_mfma_f32_16x16x32_f16 v[78:81], v[186:189], v[146:149], v[78:81]
	v_mfma_f32_16x16x32_f16 v[66:69], v[186:189], v[154:157], v[66:69]
	v_mfma_f32_16x16x32_f16 v[94:97], v[182:185], v[142:145], v[94:97]
	v_mfma_f32_16x16x32_f16 v[90:93], v[182:185], v[150:153], v[90:93]
	v_mfma_f32_16x16x32_f16 v[86:89], v[182:185], v[158:161], v[86:89]
	v_mfma_f32_16x16x32_f16 v[82:85], v[190:193], v[142:145], v[82:85]
	v_mfma_f32_16x16x32_f16 v[78:81], v[190:193], v[150:153], v[78:81]
	v_mfma_f32_16x16x32_f16 v[66:69], v[190:193], v[158:161], v[66:69]
	s_setprio 0
	s_barrier
	v_lshl_add_u64 v[220:221], v[102:103], 0, s[2:3]
	v_readfirstlane_b32 s5, v119
	v_lshl_add_u64 v[222:223], v[220:221], 0, s[80:81]
	s_mov_b32 m0, s5
	v_add_u32_e32 v176, 0x2000, v119
	ds_read_b128 v[194:197], v134
	ds_read_b128 v[198:201], v134 offset:1024
	ds_read_b128 v[202:205], v134 offset:2048
	ds_read_b128 v[206:209], v134 offset:3072
	ds_read_b128 v[210:213], v134 offset:4096
	ds_read_b128 v[214:217], v134 offset:5120
	global_load_lds_dwordx4 v[222:223], off
	v_lshl_add_u64 v[222:223], v[104:105], 0, s[2:3]
	v_readfirstlane_b32 s5, v176
	v_lshl_add_u64 v[224:225], v[222:223], 0, s[80:81]
	s_mov_b32 m0, s5
	s_nop 0
	global_load_lds_dwordx4 v[224:225], off
	s_barrier
	s_waitcnt lgkmcnt(0)
	s_setprio 1
	s_waitcnt lgkmcnt(0)
	v_mfma_f32_16x16x32_f16 v[22:25], v[162:165], v[194:197], v[22:25]
	v_mfma_f32_16x16x32_f16 v[18:21], v[162:165], v[202:205], v[18:21]
	v_mfma_f32_16x16x32_f16 v[14:17], v[162:165], v[210:213], v[14:17]
	v_mfma_f32_16x16x32_f16 v[10:13], v[186:189], v[194:197], v[10:13]
	v_mfma_f32_16x16x32_f16 v[6:9], v[186:189], v[202:205], v[6:9]
	v_mfma_f32_16x16x32_f16 v[2:5], v[186:189], v[210:213], v[2:5]
	v_mfma_f32_16x16x32_f16 v[22:25], v[182:185], v[198:201], v[22:25]
	v_mfma_f32_16x16x32_f16 v[18:21], v[182:185], v[206:209], v[18:21]
	v_mfma_f32_16x16x32_f16 v[14:17], v[182:185], v[214:217], v[14:17]
	v_mfma_f32_16x16x32_f16 v[10:13], v[190:193], v[198:201], v[10:13]
	v_mfma_f32_16x16x32_f16 v[6:9], v[190:193], v[206:209], v[6:9]
	v_mfma_f32_16x16x32_f16 v[2:5], v[190:193], v[214:217], v[2:5]
	s_setprio 0
	v_readfirstlane_b32 s5, v120
	v_lshl_add_u64 v[224:225], v[166:167], 0, s[80:81]
	s_mov_b32 m0, s5
	v_readfirstlane_b32 s5, v122
	s_barrier
	ds_read_b128 v[162:165], v121 offset:16384
	ds_read_b128 v[182:185], v121 offset:17408
	ds_read_b128 v[186:189], v108 offset:16384
	ds_read_b128 v[190:193], v108 offset:17408
	global_load_lds_dwordx4 v[224:225], off
	v_lshl_add_u64 v[224:225], v[218:219], 0, s[80:81]
	s_mov_b32 m0, s5
	s_nop 0
	global_load_lds_dwordx4 v[224:225], off
	s_barrier
	s_waitcnt lgkmcnt(0)
	s_setprio 1
	s_waitcnt lgkmcnt(0)
	v_mfma_f32_16x16x32_f16 v[26:29], v[162:165], v[138:141], v[26:29]
	v_mfma_f32_16x16x32_f16 v[30:33], v[162:165], v[146:149], v[30:33]
	v_mfma_f32_16x16x32_f16 v[34:37], v[162:165], v[154:157], v[34:37]
	v_mfma_f32_16x16x32_f16 v[38:41], v[186:189], v[138:141], v[38:41]
	v_mfma_f32_16x16x32_f16 v[46:49], v[186:189], v[146:149], v[46:49]
	v_mfma_f32_16x16x32_f16 v[54:57], v[186:189], v[154:157], v[54:57]
	v_mfma_f32_16x16x32_f16 v[26:29], v[182:185], v[142:145], v[26:29]
	v_mfma_f32_16x16x32_f16 v[30:33], v[182:185], v[150:153], v[30:33]
	v_mfma_f32_16x16x32_f16 v[34:37], v[182:185], v[158:161], v[34:37]
	v_mfma_f32_16x16x32_f16 v[38:41], v[190:193], v[142:145], v[38:41]
	v_mfma_f32_16x16x32_f16 v[46:49], v[190:193], v[150:153], v[46:49]
	v_mfma_f32_16x16x32_f16 v[54:57], v[190:193], v[158:161], v[54:57]
	s_setprio 0
	s_barrier
	v_lshl_add_u64 v[224:225], v[114:115], 0, s[2:3]
	v_readfirstlane_b32 s5, v123
	v_add_u32_e32 v140, 0x2000, v123
	v_lshl_add_u64 v[138:139], v[224:225], 0, s[82:83]
	s_mov_b32 m0, s5
	v_lshl_add_u64 v[226:227], v[116:117], 0, s[2:3]
	v_readfirstlane_b32 s5, v140
	global_load_lds_dwordx4 v[138:139], off
	v_lshl_add_u64 v[138:139], v[226:227], 0, s[82:83]
	s_mov_b32 m0, s5
	s_nop 0
	global_load_lds_dwordx4 v[138:139], off
	s_waitcnt vmcnt(6)
	s_barrier
	s_setprio 1
	v_mfma_f32_16x16x32_f16 v[42:45], v[162:165], v[194:197], v[42:45]
	v_mfma_f32_16x16x32_f16 v[50:53], v[162:165], v[202:205], v[50:53]
	v_mfma_f32_16x16x32_f16 v[58:61], v[162:165], v[210:213], v[58:61]
	v_mfma_f32_16x16x32_f16 v[62:65], v[186:189], v[194:197], v[62:65]
	v_mfma_f32_16x16x32_f16 v[70:73], v[186:189], v[202:205], v[70:73]
	v_mfma_f32_16x16x32_f16 v[74:77], v[186:189], v[210:213], v[74:77]
	v_mfma_f32_16x16x32_f16 v[42:45], v[182:185], v[198:201], v[42:45]
	v_mfma_f32_16x16x32_f16 v[50:53], v[182:185], v[206:209], v[50:53]
	v_mfma_f32_16x16x32_f16 v[58:61], v[182:185], v[214:217], v[58:61]
	v_mfma_f32_16x16x32_f16 v[62:65], v[190:193], v[198:201], v[62:65]
	v_mfma_f32_16x16x32_f16 v[70:73], v[190:193], v[206:209], v[70:73]
	v_mfma_f32_16x16x32_f16 v[74:77], v[190:193], v[214:217], v[74:77]
	s_setprio 0
	s_barrier
	ds_read_b128 v[138:141], v127
	ds_read_b128 v[142:145], v127 offset:1024
	ds_read_b128 v[146:149], v127 offset:2048
	ds_read_b128 v[150:153], v127 offset:3072
	ds_read_b128 v[154:157], v127 offset:4096
	ds_read_b128 v[158:161], v127 offset:5120
	v_readfirstlane_b32 s5, v125
	v_lshl_add_u64 v[194:195], v[166:167], 0, s[84:85]
	s_mov_b32 m0, s5
	v_readfirstlane_b32 s5, v126
	ds_read_b128 v[162:165], v121 offset:32768
	ds_read_b128 v[182:185], v121 offset:33792
	ds_read_b128 v[186:189], v108 offset:32768
	ds_read_b128 v[190:193], v108 offset:33792
	global_load_lds_dwordx4 v[194:195], off
	v_lshl_add_u64 v[194:195], v[218:219], 0, s[84:85]
	s_mov_b32 m0, s5
	s_nop 0
	global_load_lds_dwordx4 v[194:195], off
	s_waitcnt lgkmcnt(4)
	s_barrier
	s_waitcnt lgkmcnt(0)
	s_setprio 1
	s_waitcnt lgkmcnt(0)
	v_mfma_f32_16x16x32_f16 v[94:97], v[162:165], v[138:141], v[94:97]
	v_mfma_f32_16x16x32_f16 v[90:93], v[162:165], v[146:149], v[90:93]
	v_mfma_f32_16x16x32_f16 v[86:89], v[162:165], v[154:157], v[86:89]
	v_mfma_f32_16x16x32_f16 v[82:85], v[186:189], v[138:141], v[82:85]
	v_mfma_f32_16x16x32_f16 v[78:81], v[186:189], v[146:149], v[78:81]
	v_mfma_f32_16x16x32_f16 v[66:69], v[186:189], v[154:157], v[66:69]
	v_mfma_f32_16x16x32_f16 v[94:97], v[182:185], v[142:145], v[94:97]
	v_mfma_f32_16x16x32_f16 v[90:93], v[182:185], v[150:153], v[90:93]
	v_mfma_f32_16x16x32_f16 v[86:89], v[182:185], v[158:161], v[86:89]
	v_mfma_f32_16x16x32_f16 v[82:85], v[190:193], v[142:145], v[82:85]
	v_mfma_f32_16x16x32_f16 v[78:81], v[190:193], v[150:153], v[78:81]
	v_mfma_f32_16x16x32_f16 v[66:69], v[190:193], v[158:161], v[66:69]
	s_setprio 0
	s_barrier
	v_readfirstlane_b32 s5, v128
	v_lshl_add_u64 v[220:221], v[220:221], 0, s[86:87]
	s_mov_b32 m0, s5
	v_readfirstlane_b32 s5, v129
	ds_read_b128 v[194:197], v124
	ds_read_b128 v[198:201], v124 offset:1024
	ds_read_b128 v[202:205], v124 offset:2048
	ds_read_b128 v[206:209], v124 offset:3072
	ds_read_b128 v[210:213], v124 offset:4096
	ds_read_b128 v[214:217], v124 offset:5120
	global_load_lds_dwordx4 v[220:221], off
	v_lshl_add_u64 v[220:221], v[222:223], 0, s[86:87]
	s_mov_b32 m0, s5
	s_nop 0
	global_load_lds_dwordx4 v[220:221], off
	s_barrier
	s_waitcnt lgkmcnt(0)
	s_setprio 1
	s_waitcnt lgkmcnt(0)
	v_mfma_f32_16x16x32_f16 v[22:25], v[162:165], v[194:197], v[22:25]
	v_mfma_f32_16x16x32_f16 v[18:21], v[162:165], v[202:205], v[18:21]
	v_mfma_f32_16x16x32_f16 v[14:17], v[162:165], v[210:213], v[14:17]
	v_mfma_f32_16x16x32_f16 v[10:13], v[186:189], v[194:197], v[10:13]
	v_mfma_f32_16x16x32_f16 v[6:9], v[186:189], v[202:205], v[6:9]
	v_mfma_f32_16x16x32_f16 v[2:5], v[186:189], v[210:213], v[2:5]
	v_mfma_f32_16x16x32_f16 v[22:25], v[182:185], v[198:201], v[22:25]
	v_mfma_f32_16x16x32_f16 v[18:21], v[182:185], v[206:209], v[18:21]
	v_mfma_f32_16x16x32_f16 v[14:17], v[182:185], v[214:217], v[14:17]
	v_mfma_f32_16x16x32_f16 v[10:13], v[190:193], v[198:201], v[10:13]
	v_mfma_f32_16x16x32_f16 v[6:9], v[190:193], v[206:209], v[6:9]
	v_mfma_f32_16x16x32_f16 v[2:5], v[190:193], v[214:217], v[2:5]
	s_setprio 0
	v_readfirstlane_b32 s5, v130
	v_lshl_add_u64 v[166:167], v[166:167], 0, s[86:87]
	s_mov_b32 m0, s5
	v_readfirstlane_b32 s5, v131
	s_barrier
	ds_read_b128 v[162:165], v121 offset:49152
	ds_read_b128 v[182:185], v121 offset:50176
	ds_read_b128 v[186:189], v108 offset:49152
	ds_read_b128 v[190:193], v108 offset:50176
	global_load_lds_dwordx4 v[166:167], off
	v_lshl_add_u64 v[166:167], v[218:219], 0, s[86:87]
	s_mov_b32 m0, s5
	s_nop 0
	global_load_lds_dwordx4 v[166:167], off
	s_barrier
	s_waitcnt lgkmcnt(0)
	s_setprio 1
	s_waitcnt lgkmcnt(0)
	v_mfma_f32_16x16x32_f16 v[26:29], v[162:165], v[138:141], v[26:29]
	v_mfma_f32_16x16x32_f16 v[30:33], v[162:165], v[146:149], v[30:33]
	v_mfma_f32_16x16x32_f16 v[34:37], v[162:165], v[154:157], v[34:37]
	v_mfma_f32_16x16x32_f16 v[38:41], v[186:189], v[138:141], v[38:41]
	v_mfma_f32_16x16x32_f16 v[46:49], v[186:189], v[146:149], v[46:49]
	v_mfma_f32_16x16x32_f16 v[54:57], v[186:189], v[154:157], v[54:57]
	v_mfma_f32_16x16x32_f16 v[26:29], v[182:185], v[142:145], v[26:29]
	v_mfma_f32_16x16x32_f16 v[30:33], v[182:185], v[150:153], v[30:33]
	v_mfma_f32_16x16x32_f16 v[34:37], v[182:185], v[158:161], v[34:37]
	v_mfma_f32_16x16x32_f16 v[38:41], v[190:193], v[142:145], v[38:41]
	v_mfma_f32_16x16x32_f16 v[46:49], v[190:193], v[150:153], v[46:49]
	v_mfma_f32_16x16x32_f16 v[54:57], v[190:193], v[158:161], v[54:57]
	s_setprio 0
	s_barrier
	v_readfirstlane_b32 s5, v132
	v_lshl_add_u64 v[138:139], v[224:225], 0, s[88:89]
	s_mov_b32 m0, s5
	v_readfirstlane_b32 s5, v133
	global_load_lds_dwordx4 v[138:139], off
	v_lshl_add_u64 v[138:139], v[226:227], 0, s[88:89]
	s_mov_b32 m0, s5
	s_nop 0
	global_load_lds_dwordx4 v[138:139], off
	s_waitcnt vmcnt(6)
	s_barrier
	s_setprio 1
	v_mfma_f32_16x16x32_f16 v[42:45], v[162:165], v[194:197], v[42:45]
	v_mfma_f32_16x16x32_f16 v[50:53], v[162:165], v[202:205], v[50:53]
	v_mfma_f32_16x16x32_f16 v[58:61], v[162:165], v[210:213], v[58:61]
	v_mfma_f32_16x16x32_f16 v[62:65], v[186:189], v[194:197], v[62:65]
	v_mfma_f32_16x16x32_f16 v[70:73], v[186:189], v[202:205], v[70:73]
	v_mfma_f32_16x16x32_f16 v[74:77], v[186:189], v[210:213], v[74:77]
	v_mfma_f32_16x16x32_f16 v[42:45], v[182:185], v[198:201], v[42:45]
	v_mfma_f32_16x16x32_f16 v[50:53], v[182:185], v[206:209], v[50:53]
	v_mfma_f32_16x16x32_f16 v[58:61], v[182:185], v[214:217], v[58:61]
	v_mfma_f32_16x16x32_f16 v[62:65], v[190:193], v[198:201], v[62:65]
	v_mfma_f32_16x16x32_f16 v[70:73], v[190:193], v[206:209], v[70:73]
	v_mfma_f32_16x16x32_f16 v[74:77], v[190:193], v[214:217], v[74:77]
	s_setprio 0
	s_add_i32 s4, s4, 2
	s_add_u32 s2, s2, 0x100
	s_addc_u32 s3, s3, 0
	s_cmp_lt_u32 s4, 8
	s_barrier
	s_cbranch_scc1 .LBB1_52
	s_and_saveexec_b64 s[100:101], s[34:35]
	s_cbranch_execz .Lpf_skip_g2
	v_lshlrev_b32_e32 v232, 5, v173
	v_mov_b32_e32 v233, 0
	v_lshl_add_u64 v[232:233], v[232:233], 2, s[64:65]
	global_atomic_add v231, v[232:233], v1, off sc0
.Lpf_skip_g2:
	s_mov_b64 exec, s[100:101]
	s_mov_b64 s[4:5], 0x580
	v_readfirstlane_b32 s2, v136
	v_lshl_add_u64 v[98:99], v[98:99], 0, s[4:5]
	s_mov_b32 m0, s2
	v_readfirstlane_b32 s2, v137
	ds_read_b128 v[102:105], v135
	ds_read_b128 v[110:113], v135 offset:1024
	ds_read_b128 v[114:117], v135 offset:2048
	ds_read_b128 v[128:131], v135 offset:3072
	ds_read_b128 v[138:141], v135 offset:4096
	ds_read_b128 v[142:145], v135 offset:5120
	ds_read_b128 v[146:149], v121
	ds_read_b128 v[150:153], v121 offset:1024
	ds_read_b128 v[154:157], v108
	ds_read_b128 v[158:161], v108 offset:1024
	global_load_lds_dwordx4 v[98:99], off
	v_lshl_add_u64 v[98:99], v[100:101], 0, s[4:5]
	s_mov_b32 m0, s2
	s_nop 0
	global_load_lds_dwordx4 v[98:99], off
	s_barrier
	s_waitcnt lgkmcnt(0)
	s_setprio 1
	s_waitcnt lgkmcnt(0)
	v_mfma_f32_16x16x32_f16 v[94:97], v[146:149], v[102:105], v[94:97]
	v_mfma_f32_16x16x32_f16 v[90:93], v[146:149], v[114:117], v[90:93]
	v_mfma_f32_16x16x32_f16 v[86:89], v[146:149], v[138:141], v[86:89]
	v_mfma_f32_16x16x32_f16 v[82:85], v[154:157], v[102:105], v[82:85]
	v_mfma_f32_16x16x32_f16 v[78:81], v[154:157], v[114:117], v[78:81]
	v_mfma_f32_16x16x32_f16 v[66:69], v[154:157], v[138:141], v[66:69]
	v_mfma_f32_16x16x32_f16 v[94:97], v[150:153], v[110:113], v[94:97]
	v_mfma_f32_16x16x32_f16 v[90:93], v[150:153], v[128:131], v[90:93]
	v_mfma_f32_16x16x32_f16 v[86:89], v[150:153], v[142:145], v[86:89]
	v_mfma_f32_16x16x32_f16 v[82:85], v[158:161], v[110:113], v[82:85]
	v_mfma_f32_16x16x32_f16 v[98:101], v[158:161], v[128:131], v[78:81]
	v_mfma_f32_16x16x32_f16 v[66:69], v[158:161], v[142:145], v[66:69]
	s_setprio 0
	s_barrier
	ds_read_b128 v[78:81], v134
	ds_read_b128 v[162:165], v134 offset:1024
	ds_read_b128 v[182:185], v134 offset:2048
	ds_read_b128 v[186:189], v134 offset:3072
	ds_read_b128 v[190:193], v134 offset:4096
	ds_read_b128 v[132:135], v134 offset:5120
	s_barrier
	s_waitcnt lgkmcnt(0)
	s_setprio 1
	s_waitcnt lgkmcnt(0)
	v_mfma_f32_16x16x32_f16 v[22:25], v[146:149], v[78:81], v[22:25]
	v_mfma_f32_16x16x32_f16 v[18:21], v[146:149], v[182:185], v[18:21]
	v_mfma_f32_16x16x32_f16 v[14:17], v[146:149], v[190:193], v[14:17]
	v_mfma_f32_16x16x32_f16 v[10:13], v[154:157], v[78:81], v[10:13]
	v_mfma_f32_16x16x32_f16 v[6:9], v[154:157], v[182:185], v[6:9]
	v_mfma_f32_16x16x32_f16 v[2:5], v[154:157], v[190:193], v[2:5]
	v_mfma_f32_16x16x32_f16 v[22:25], v[150:153], v[162:165], v[22:25]
	v_mfma_f32_16x16x32_f16 v[18:21], v[150:153], v[186:189], v[18:21]
	v_mfma_f32_16x16x32_f16 v[14:17], v[150:153], v[132:135], v[14:17]
	v_mfma_f32_16x16x32_f16 v[10:13], v[158:161], v[162:165], v[10:13]
	v_mfma_f32_16x16x32_f16 v[6:9], v[158:161], v[186:189], v[6:9]
	v_mfma_f32_16x16x32_f16 v[2:5], v[158:161], v[132:135], v[2:5]
	s_setprio 0
	s_barrier
	ds_read_b128 v[146:149], v121 offset:16384
	ds_read_b128 v[150:153], v121 offset:17408
	ds_read_b128 v[154:157], v108 offset:16384
	ds_read_b128 v[158:161], v108 offset:17408
	s_waitcnt vmcnt(4)
	s_barrier
	s_waitcnt lgkmcnt(0)
	s_setprio 1
	s_waitcnt lgkmcnt(0)
	v_mfma_f32_16x16x32_f16 v[26:29], v[146:149], v[102:105], v[26:29]
	v_mfma_f32_16x16x32_f16 v[30:33], v[146:149], v[114:117], v[30:33]
	v_mfma_f32_16x16x32_f16 v[34:37], v[146:149], v[138:141], v[34:37]
	v_mfma_f32_16x16x32_f16 v[38:41], v[154:157], v[102:105], v[38:41]
	v_mfma_f32_16x16x32_f16 v[46:49], v[154:157], v[114:117], v[46:49]
	v_mfma_f32_16x16x32_f16 v[26:29], v[150:153], v[110:113], v[26:29]
	v_mfma_f32_16x16x32_f16 v[30:33], v[150:153], v[128:131], v[30:33]
	v_mfma_f32_16x16x32_f16 v[34:37], v[150:153], v[142:145], v[34:37]
	v_mfma_f32_16x16x32_f16 v[38:41], v[158:161], v[110:113], v[38:41]
	v_mfma_f32_16x16x32_f16 v[46:49], v[158:161], v[128:131], v[46:49]
	v_mfma_f32_16x16x32_f16 v[54:57], v[154:157], v[138:141], v[54:57]
	v_mfma_f32_16x16x32_f16 v[54:57], v[158:161], v[142:145], v[54:57]
	s_setprio 0
	s_setprio 1
	v_mfma_f32_16x16x32_f16 v[58:61], v[146:149], v[190:193], v[58:61]
	v_mfma_f32_16x16x32_f16 v[110:113], v[150:153], v[132:135], v[58:61]
	v_mfma_f32_16x16x32_f16 v[58:61], v[154:157], v[78:81], v[62:65]
	v_mfma_f32_16x16x32_f16 v[42:45], v[146:149], v[78:81], v[42:45]
	v_mfma_f32_16x16x32_f16 v[114:117], v[158:161], v[162:165], v[58:61]
	v_mfma_f32_16x16x32_f16 v[58:61], v[154:157], v[182:185], v[70:73]
	v_mfma_f32_16x16x32_f16 v[42:45], v[150:153], v[162:165], v[42:45]
	v_mfma_f32_16x16x32_f16 v[50:53], v[146:149], v[182:185], v[50:53]
	v_mfma_f32_16x16x32_f16 v[128:131], v[158:161], v[186:189], v[58:61]
	v_mfma_f32_16x16x32_f16 v[58:61], v[154:157], v[190:193], v[74:77]
	v_mfma_f32_16x16x32_f16 v[50:53], v[150:153], v[186:189], v[50:53]
	v_mfma_f32_16x16x32_f16 v[132:135], v[158:161], v[132:135], v[58:61]
	s_setprio 0
	s_barrier
	ds_read_b128 v[136:139], v127
	ds_read_b128 v[140:143], v127 offset:1024
	ds_read_b128 v[144:147], v127 offset:2048
	ds_read_b128 v[148:151], v127 offset:3072
	ds_read_b128 v[152:155], v127 offset:4096
	ds_read_b128 v[156:159], v127 offset:5120
	ds_read_b128 v[74:77], v121 offset:32768
	ds_read_b128 v[160:163], v121 offset:33792
	ds_read_b128 v[164:167], v108 offset:32768
	ds_read_b128 v[182:185], v108 offset:33792
	s_waitcnt vmcnt(2)
	s_barrier
	s_waitcnt lgkmcnt(0)
	s_setprio 1
	s_waitcnt lgkmcnt(0)
	v_mfma_f32_16x16x32_f16 v[62:65], v[74:77], v[144:147], v[90:93]
	v_mfma_f32_16x16x32_f16 v[70:73], v[164:167], v[136:139], v[82:85]
	v_mfma_f32_16x16x32_f16 v[58:61], v[74:77], v[136:139], v[94:97]
	v_mfma_f32_16x16x32_f16 v[78:81], v[160:163], v[148:151], v[62:65]
	v_mfma_f32_16x16x32_f16 v[62:65], v[74:77], v[152:155], v[86:89]
	v_mfma_f32_16x16x32_f16 v[102:105], v[182:185], v[140:143], v[70:73]
	v_mfma_f32_16x16x32_f16 v[70:73], v[164:167], v[144:147], v[98:101]
	v_mfma_f32_16x16x32_f16 v[66:69], v[164:167], v[152:155], v[66:69]
	v_mfma_f32_16x16x32_f16 v[58:61], v[160:163], v[140:143], v[58:61]
	v_mfma_f32_16x16x32_f16 v[62:65], v[160:163], v[156:159], v[62:65]
	v_mfma_f32_16x16x32_f16 v[86:89], v[182:185], v[148:151], v[70:73]
	v_mfma_f32_16x16x32_f16 v[70:73], v[182:185], v[156:159], v[66:69]
	s_setprio 0
	s_barrier
	ds_read_b128 v[186:189], v124
	ds_read_b128 v[190:193], v124 offset:1024
	ds_read_b128 v[194:197], v124 offset:2048
	ds_read_b128 v[198:201], v124 offset:3072
	ds_read_b128 v[202:205], v124 offset:4096
	ds_read_b128 v[122:125], v124 offset:5120
	s_waitcnt vmcnt(0)
	s_barrier
	s_waitcnt lgkmcnt(0)
	s_setprio 1
	s_waitcnt lgkmcnt(0)
	v_mfma_f32_16x16x32_f16 v[22:25], v[74:77], v[186:189], v[22:25]
	v_mfma_f32_16x16x32_f16 v[18:21], v[74:77], v[194:197], v[18:21]
	v_mfma_f32_16x16x32_f16 v[14:17], v[74:77], v[202:205], v[14:17]
	v_mfma_f32_16x16x32_f16 v[10:13], v[164:167], v[186:189], v[10:13]
	v_mfma_f32_16x16x32_f16 v[6:9], v[164:167], v[194:197], v[6:9]
	v_mfma_f32_16x16x32_f16 v[2:5], v[164:167], v[202:205], v[2:5]
	v_mfma_f32_16x16x32_f16 v[94:97], v[160:163], v[190:193], v[22:25]
	v_mfma_f32_16x16x32_f16 v[82:85], v[160:163], v[198:201], v[18:21]
	v_mfma_f32_16x16x32_f16 v[66:69], v[160:163], v[122:125], v[14:17]
	v_mfma_f32_16x16x32_f16 v[98:101], v[182:185], v[190:193], v[10:13]
	v_mfma_f32_16x16x32_f16 v[90:93], v[182:185], v[198:201], v[6:9]
	v_mfma_f32_16x16x32_f16 v[74:77], v[182:185], v[122:125], v[2:5]
	s_setprio 0
	s_barrier
	ds_read_b128 v[10:13], v121 offset:49152
	ds_read_b128 v[160:163], v121 offset:50176
	ds_read_b128 v[164:167], v108 offset:49152
	ds_read_b128 v[182:185], v108 offset:50176
	s_barrier
	s_waitcnt lgkmcnt(0)
	s_setprio 1
	s_waitcnt lgkmcnt(0)
	v_mfma_f32_16x16x32_f16 v[2:5], v[10:13], v[136:139], v[26:29]
	v_mfma_f32_16x16x32_f16 v[18:21], v[164:167], v[136:139], v[38:41]
	v_mfma_f32_16x16x32_f16 v[14:17], v[160:163], v[140:143], v[2:5]
	v_mfma_f32_16x16x32_f16 v[2:5], v[10:13], v[144:147], v[30:33]
	v_mfma_f32_16x16x32_f16 v[38:41], v[182:185], v[140:143], v[18:21]
	v_mfma_f32_16x16x32_f16 v[18:21], v[164:167], v[144:147], v[46:49]
	v_mfma_f32_16x16x32_f16 v[6:9], v[160:163], v[148:151], v[2:5]
	v_mfma_f32_16x16x32_f16 v[2:5], v[10:13], v[152:155], v[34:37]
	v_mfma_f32_16x16x32_f16 v[26:29], v[182:185], v[148:151], v[18:21]
	v_mfma_f32_16x16x32_f16 v[18:21], v[164:167], v[152:155], v[54:57]
	v_mfma_f32_16x16x32_f16 v[2:5], v[160:163], v[156:159], v[2:5]
	v_mfma_f32_16x16x32_f16 v[18:21], v[182:185], v[156:159], v[18:21]
	s_setprio 0
	s_setprio 1
	v_mfma_f32_16x16x32_f16 v[34:37], v[164:167], v[186:189], v[114:117]
	v_mfma_f32_16x16x32_f16 v[22:25], v[10:13], v[186:189], v[42:45]
	v_mfma_f32_16x16x32_f16 v[46:49], v[182:185], v[190:193], v[34:37]
	v_mfma_f32_16x16x32_f16 v[34:37], v[164:167], v[194:197], v[128:131]
	v_mfma_f32_16x16x32_f16 v[30:33], v[160:163], v[190:193], v[22:25]
	v_mfma_f32_16x16x32_f16 v[22:25], v[10:13], v[194:197], v[50:53]
	v_mfma_f32_16x16x32_f16 v[10:13], v[10:13], v[202:205], v[110:113]
	v_mfma_f32_16x16x32_f16 v[42:45], v[182:185], v[198:201], v[34:37]
	v_mfma_f32_16x16x32_f16 v[34:37], v[164:167], v[202:205], v[132:135]
	v_mfma_f32_16x16x32_f16 v[22:25], v[160:163], v[198:201], v[22:25]
	v_mfma_f32_16x16x32_f16 v[10:13], v[160:163], v[122:125], v[10:13]
	v_mfma_f32_16x16x32_f16 v[34:37], v[182:185], v[122:125], v[34:37]
	s_setprio 0
	s_movk_i32 s2, 0x100
	v_cmp_gt_u32_e32 vcc, s2, v175
	s_barrier
	s_and_saveexec_b64 s[2:3], vcc
	s_cbranch_execz .LBB1_55
	s_barrier

.LBB1_66:
	ds_read_b128 v[148:151], v144
	ds_read_b128 v[152:155], v144 offset:1024
	ds_read_b128 v[156:159], v144 offset:2048
	ds_read_b128 v[160:163], v144 offset:3072
	ds_read_b128 v[164:167], v144 offset:4096
	ds_read_b128 v[174:177], v144 offset:5120
	v_add_u32_e32 v145, 0xc000, v129
	v_lshl_add_u64 v[218:219], v[112:113], 0, s[0:1]
	v_readfirstlane_b32 s3, v145
	v_lshl_add_u64 v[146:147], v[218:219], 0, s[78:79]
	s_mov_b32 m0, s3
	ds_read_b128 v[178:181], v130
	ds_read_b128 v[182:185], v130 offset:1024
	ds_read_b128 v[186:189], v108
	ds_read_b128 v[190:193], v108 offset:1024
	global_load_lds_dwordx4 v[146:147], off
	v_add_u32_e32 v146, 0xe000, v129
	v_lshl_add_u64 v[220:221], v[114:115], 0, s[0:1]
	v_readfirstlane_b32 s3, v146
	v_lshl_add_u64 v[194:195], v[220:221], 0, s[78:79]
	s_mov_b32 m0, s3
	s_nop 0
	global_load_lds_dwordx4 v[194:195], off
	s_waitcnt lgkmcnt(4)
	s_barrier
	s_waitcnt lgkmcnt(0)
	s_setprio 1
	s_waitcnt lgkmcnt(0)
	v_mfma_f32_16x16x32_f16 v[94:97], v[178:181], v[148:151], v[94:97]
	v_mfma_f32_16x16x32_f16 v[90:93], v[178:181], v[156:159], v[90:93]
	v_mfma_f32_16x16x32_f16 v[86:89], v[178:181], v[164:167], v[86:89]
	v_mfma_f32_16x16x32_f16 v[74:77], v[186:189], v[148:151], v[74:77]
	v_mfma_f32_16x16x32_f16 v[46:49], v[186:189], v[156:159], v[46:49]
	v_mfma_f32_16x16x32_f16 v[18:21], v[186:189], v[164:167], v[18:21]
	v_mfma_f32_16x16x32_f16 v[94:97], v[182:185], v[152:155], v[94:97]
	v_mfma_f32_16x16x32_f16 v[90:93], v[182:185], v[160:163], v[90:93]
	v_mfma_f32_16x16x32_f16 v[86:89], v[182:185], v[174:177], v[86:89]
	v_mfma_f32_16x16x32_f16 v[74:77], v[190:193], v[152:155], v[74:77]
	v_mfma_f32_16x16x32_f16 v[46:49], v[190:193], v[160:163], v[46:49]
	v_mfma_f32_16x16x32_f16 v[18:21], v[190:193], v[174:177], v[18:21]
	s_setprio 0
	s_barrier
	v_lshl_add_u64 v[222:223], v[104:105], 0, s[0:1]
	v_readfirstlane_b32 s3, v128
	v_lshl_add_u64 v[224:225], v[222:223], 0, s[80:81]
	s_mov_b32 m0, s3
	v_add_u32_e32 v147, 0x2000, v128
	ds_read_b128 v[194:197], v143
	ds_read_b128 v[198:201], v143 offset:1024
	ds_read_b128 v[202:205], v143 offset:2048
	ds_read_b128 v[206:209], v143 offset:3072
	ds_read_b128 v[210:213], v143 offset:4096
	ds_read_b128 v[214:217], v143 offset:5120
	global_load_lds_dwordx4 v[224:225], off
	v_lshl_add_u64 v[224:225], v[110:111], 0, s[0:1]
	v_readfirstlane_b32 s3, v147
	v_lshl_add_u64 v[226:227], v[224:225], 0, s[80:81]
	s_mov_b32 m0, s3
	s_nop 0
	global_load_lds_dwordx4 v[226:227], off
	s_barrier
	s_waitcnt lgkmcnt(0)
	s_setprio 1
	s_waitcnt lgkmcnt(0)
	v_mfma_f32_16x16x32_f16 v[10:13], v[178:181], v[194:197], v[10:13]
	v_mfma_f32_16x16x32_f16 v[6:9], v[178:181], v[202:205], v[6:9]
	v_mfma_f32_16x16x32_f16 v[2:5], v[178:181], v[210:213], v[2:5]
	v_mfma_f32_16x16x32_f16 v[26:29], v[186:189], v[194:197], v[26:29]
	v_mfma_f32_16x16x32_f16 v[34:37], v[186:189], v[202:205], v[34:37]
	v_mfma_f32_16x16x32_f16 v[50:53], v[186:189], v[210:213], v[50:53]
	v_mfma_f32_16x16x32_f16 v[10:13], v[182:185], v[198:201], v[10:13]
	v_mfma_f32_16x16x32_f16 v[6:9], v[182:185], v[206:209], v[6:9]
	v_mfma_f32_16x16x32_f16 v[2:5], v[182:185], v[214:217], v[2:5]
	v_mfma_f32_16x16x32_f16 v[26:29], v[190:193], v[198:201], v[26:29]
	v_mfma_f32_16x16x32_f16 v[34:37], v[190:193], v[206:209], v[34:37]
	v_mfma_f32_16x16x32_f16 v[50:53], v[190:193], v[214:217], v[50:53]
	s_setprio 0
	v_readfirstlane_b32 s3, v129
	v_lshl_add_u64 v[226:227], v[218:219], 0, s[80:81]
	s_mov_b32 m0, s3
	v_readfirstlane_b32 s3, v131
	s_barrier
	ds_read_b128 v[178:181], v130 offset:16384
	ds_read_b128 v[182:185], v130 offset:17408
	ds_read_b128 v[186:189], v108 offset:16384
	ds_read_b128 v[190:193], v108 offset:17408
	global_load_lds_dwordx4 v[226:227], off
	v_lshl_add_u64 v[226:227], v[220:221], 0, s[80:81]
	s_mov_b32 m0, s3
	s_nop 0
	global_load_lds_dwordx4 v[226:227], off
	s_barrier
	s_waitcnt lgkmcnt(0)
	s_setprio 1
	s_waitcnt lgkmcnt(0)
	v_mfma_f32_16x16x32_f16 v[14:17], v[178:181], v[148:151], v[14:17]
	v_mfma_f32_16x16x32_f16 v[22:25], v[178:181], v[156:159], v[22:25]
	v_mfma_f32_16x16x32_f16 v[30:33], v[178:181], v[164:167], v[30:33]
	v_mfma_f32_16x16x32_f16 v[38:41], v[186:189], v[148:151], v[38:41]
	v_mfma_f32_16x16x32_f16 v[54:57], v[186:189], v[156:159], v[54:57]
	v_mfma_f32_16x16x32_f16 v[62:65], v[186:189], v[164:167], v[62:65]
	v_mfma_f32_16x16x32_f16 v[14:17], v[182:185], v[152:155], v[14:17]
	v_mfma_f32_16x16x32_f16 v[22:25], v[182:185], v[160:163], v[22:25]
	v_mfma_f32_16x16x32_f16 v[30:33], v[182:185], v[174:177], v[30:33]
	v_mfma_f32_16x16x32_f16 v[38:41], v[190:193], v[152:155], v[38:41]
	v_mfma_f32_16x16x32_f16 v[54:57], v[190:193], v[160:163], v[54:57]
	v_mfma_f32_16x16x32_f16 v[62:65], v[190:193], v[174:177], v[62:65]
	s_setprio 0
	s_barrier
	v_lshl_add_u64 v[226:227], v[116:117], 0, s[0:1]
	v_readfirstlane_b32 s3, v132
	v_add_u32_e32 v147, 0x2000, v132
	v_lshl_add_u64 v[148:149], v[226:227], 0, s[82:83]
	s_mov_b32 m0, s3
	v_lshl_add_u64 v[228:229], v[118:119], 0, s[0:1]
	v_readfirstlane_b32 s3, v147
	global_load_lds_dwordx4 v[148:149], off
	v_lshl_add_u64 v[148:149], v[228:229], 0, s[82:83]
	s_mov_b32 m0, s3
	s_nop 0
	global_load_lds_dwordx4 v[148:149], off
	s_waitcnt vmcnt(6)
	s_barrier
	s_setprio 1
	v_mfma_f32_16x16x32_f16 v[42:45], v[178:181], v[194:197], v[42:45]
	v_mfma_f32_16x16x32_f16 v[58:61], v[178:181], v[202:205], v[58:61]
	v_mfma_f32_16x16x32_f16 v[66:69], v[178:181], v[210:213], v[66:69]
	v_mfma_f32_16x16x32_f16 v[70:73], v[186:189], v[194:197], v[70:73]
	v_mfma_f32_16x16x32_f16 v[78:81], v[186:189], v[202:205], v[78:81]
	v_mfma_f32_16x16x32_f16 v[82:85], v[186:189], v[210:213], v[82:85]
	v_mfma_f32_16x16x32_f16 v[42:45], v[182:185], v[198:201], v[42:45]
	v_mfma_f32_16x16x32_f16 v[58:61], v[182:185], v[206:209], v[58:61]
	v_mfma_f32_16x16x32_f16 v[66:69], v[182:185], v[214:217], v[66:69]
	v_mfma_f32_16x16x32_f16 v[70:73], v[190:193], v[198:201], v[70:73]
	v_mfma_f32_16x16x32_f16 v[78:81], v[190:193], v[206:209], v[78:81]
	v_mfma_f32_16x16x32_f16 v[82:85], v[190:193], v[214:217], v[82:85]
	s_setprio 0
	s_barrier
	ds_read_b128 v[148:151], v136
	ds_read_b128 v[152:155], v136 offset:1024
	ds_read_b128 v[156:159], v136 offset:2048
	ds_read_b128 v[160:163], v136 offset:3072
	ds_read_b128 v[164:167], v136 offset:4096
	ds_read_b128 v[174:177], v136 offset:5120
	v_readfirstlane_b32 s3, v134
	v_lshl_add_u64 v[194:195], v[218:219], 0, s[84:85]
	s_mov_b32 m0, s3
	v_readfirstlane_b32 s3, v135
	ds_read_b128 v[178:181], v130 offset:32768
	ds_read_b128 v[182:185], v130 offset:33792
	ds_read_b128 v[186:189], v108 offset:32768
	ds_read_b128 v[190:193], v108 offset:33792
	global_load_lds_dwordx4 v[194:195], off
	v_lshl_add_u64 v[194:195], v[220:221], 0, s[84:85]
	s_mov_b32 m0, s3
	s_nop 0
	global_load_lds_dwordx4 v[194:195], off
	s_waitcnt lgkmcnt(4)
	s_barrier
	s_waitcnt lgkmcnt(0)
	s_setprio 1
	s_waitcnt lgkmcnt(0)
	v_mfma_f32_16x16x32_f16 v[94:97], v[178:181], v[148:151], v[94:97]
	v_mfma_f32_16x16x32_f16 v[90:93], v[178:181], v[156:159], v[90:93]
	v_mfma_f32_16x16x32_f16 v[86:89], v[178:181], v[164:167], v[86:89]
	v_mfma_f32_16x16x32_f16 v[74:77], v[186:189], v[148:151], v[74:77]
	v_mfma_f32_16x16x32_f16 v[46:49], v[186:189], v[156:159], v[46:49]
	v_mfma_f32_16x16x32_f16 v[18:21], v[186:189], v[164:167], v[18:21]
	v_mfma_f32_16x16x32_f16 v[94:97], v[182:185], v[152:155], v[94:97]
	v_mfma_f32_16x16x32_f16 v[90:93], v[182:185], v[160:163], v[90:93]
	v_mfma_f32_16x16x32_f16 v[86:89], v[182:185], v[174:177], v[86:89]
	v_mfma_f32_16x16x32_f16 v[74:77], v[190:193], v[152:155], v[74:77]
	v_mfma_f32_16x16x32_f16 v[46:49], v[190:193], v[160:163], v[46:49]
	v_mfma_f32_16x16x32_f16 v[18:21], v[190:193], v[174:177], v[18:21]
	s_setprio 0
	s_barrier
	v_readfirstlane_b32 s3, v137
	v_lshl_add_u64 v[222:223], v[222:223], 0, s[86:87]
	s_mov_b32 m0, s3
	v_readfirstlane_b32 s3, v138
	ds_read_b128 v[194:197], v133
	ds_read_b128 v[198:201], v133 offset:1024
	ds_read_b128 v[202:205], v133 offset:2048
	ds_read_b128 v[206:209], v133 offset:3072
	ds_read_b128 v[210:213], v133 offset:4096
	ds_read_b128 v[214:217], v133 offset:5120
	global_load_lds_dwordx4 v[222:223], off
	v_lshl_add_u64 v[222:223], v[224:225], 0, s[86:87]
	s_mov_b32 m0, s3
	s_nop 0
	global_load_lds_dwordx4 v[222:223], off
	s_barrier
	s_waitcnt lgkmcnt(0)
	s_setprio 1
	s_waitcnt lgkmcnt(0)
	v_mfma_f32_16x16x32_f16 v[10:13], v[178:181], v[194:197], v[10:13]
	v_mfma_f32_16x16x32_f16 v[6:9], v[178:181], v[202:205], v[6:9]
	v_mfma_f32_16x16x32_f16 v[2:5], v[178:181], v[210:213], v[2:5]
	v_mfma_f32_16x16x32_f16 v[26:29], v[186:189], v[194:197], v[26:29]
	v_mfma_f32_16x16x32_f16 v[34:37], v[186:189], v[202:205], v[34:37]
	v_mfma_f32_16x16x32_f16 v[50:53], v[186:189], v[210:213], v[50:53]
	v_mfma_f32_16x16x32_f16 v[10:13], v[182:185], v[198:201], v[10:13]
	v_mfma_f32_16x16x32_f16 v[6:9], v[182:185], v[206:209], v[6:9]
	v_mfma_f32_16x16x32_f16 v[2:5], v[182:185], v[214:217], v[2:5]
	v_mfma_f32_16x16x32_f16 v[26:29], v[190:193], v[198:201], v[26:29]
	v_mfma_f32_16x16x32_f16 v[34:37], v[190:193], v[206:209], v[34:37]
	v_mfma_f32_16x16x32_f16 v[50:53], v[190:193], v[214:217], v[50:53]
	s_setprio 0
	v_readfirstlane_b32 s3, v139
	v_lshl_add_u64 v[218:219], v[218:219], 0, s[86:87]
	s_mov_b32 m0, s3
	v_readfirstlane_b32 s3, v140
	s_barrier
	ds_read_b128 v[178:181], v130 offset:49152
	ds_read_b128 v[182:185], v130 offset:50176
	ds_read_b128 v[186:189], v108 offset:49152
	ds_read_b128 v[190:193], v108 offset:50176
	global_load_lds_dwordx4 v[218:219], off
	v_lshl_add_u64 v[218:219], v[220:221], 0, s[86:87]
	s_mov_b32 m0, s3
	s_nop 0
	global_load_lds_dwordx4 v[218:219], off
	s_barrier
	s_waitcnt lgkmcnt(0)
	s_setprio 1
	s_waitcnt lgkmcnt(0)
	v_mfma_f32_16x16x32_f16 v[14:17], v[178:181], v[148:151], v[14:17]
	v_mfma_f32_16x16x32_f16 v[22:25], v[178:181], v[156:159], v[22:25]
	v_mfma_f32_16x16x32_f16 v[30:33], v[178:181], v[164:167], v[30:33]
	v_mfma_f32_16x16x32_f16 v[38:41], v[186:189], v[148:151], v[38:41]
	v_mfma_f32_16x16x32_f16 v[54:57], v[186:189], v[156:159], v[54:57]
	v_mfma_f32_16x16x32_f16 v[62:65], v[186:189], v[164:167], v[62:65]
	v_mfma_f32_16x16x32_f16 v[14:17], v[182:185], v[152:155], v[14:17]
	v_mfma_f32_16x16x32_f16 v[22:25], v[182:185], v[160:163], v[22:25]
	v_mfma_f32_16x16x32_f16 v[30:33], v[182:185], v[174:177], v[30:33]
	v_mfma_f32_16x16x32_f16 v[38:41], v[190:193], v[152:155], v[38:41]
	v_mfma_f32_16x16x32_f16 v[54:57], v[190:193], v[160:163], v[54:57]
	v_mfma_f32_16x16x32_f16 v[62:65], v[190:193], v[174:177], v[62:65]
	s_setprio 0
	s_barrier
	v_readfirstlane_b32 s3, v141
	v_lshl_add_u64 v[148:149], v[226:227], 0, s[88:89]
	s_mov_b32 m0, s3
	v_readfirstlane_b32 s3, v142
	global_load_lds_dwordx4 v[148:149], off
	v_lshl_add_u64 v[148:149], v[228:229], 0, s[88:89]
	s_mov_b32 m0, s3
	s_nop 0
	global_load_lds_dwordx4 v[148:149], off
	s_waitcnt vmcnt(6)
	s_barrier
	s_setprio 1
	v_mfma_f32_16x16x32_f16 v[42:45], v[178:181], v[194:197], v[42:45]
	v_mfma_f32_16x16x32_f16 v[58:61], v[178:181], v[202:205], v[58:61]
	v_mfma_f32_16x16x32_f16 v[66:69], v[178:181], v[210:213], v[66:69]
	v_mfma_f32_16x16x32_f16 v[70:73], v[186:189], v[194:197], v[70:73]
	v_mfma_f32_16x16x32_f16 v[78:81], v[186:189], v[202:205], v[78:81]
	v_mfma_f32_16x16x32_f16 v[82:85], v[186:189], v[210:213], v[82:85]
	v_mfma_f32_16x16x32_f16 v[42:45], v[182:185], v[198:201], v[42:45]
	v_mfma_f32_16x16x32_f16 v[58:61], v[182:185], v[206:209], v[58:61]
	v_mfma_f32_16x16x32_f16 v[66:69], v[182:185], v[214:217], v[66:69]
	v_mfma_f32_16x16x32_f16 v[70:73], v[190:193], v[198:201], v[70:73]
	v_mfma_f32_16x16x32_f16 v[78:81], v[190:193], v[206:209], v[78:81]
	v_mfma_f32_16x16x32_f16 v[82:85], v[190:193], v[214:217], v[82:85]
	s_setprio 0
	s_add_i32 s2, s2, 2
	s_add_u32 s0, s0, 0x100
	s_addc_u32 s1, s1, 0
	s_cmp_lt_u32 s2, 8
	s_barrier
	s_cbranch_scc1 .LBB1_66
	s_and_saveexec_b64 s[100:101], s[34:35]
	s_cbranch_execz .Lpf_skip_g1
	v_lshlrev_b32_e32 v232, 5, v173
	v_mov_b32_e32 v233, 0
	v_lshl_add_u64 v[232:233], v[232:233], 2, s[64:65]
	global_atomic_add v231, v[232:233], v1, off sc0
.Lpf_skip_g1:
	s_mov_b64 exec, s[100:101]
	s_mov_b64 s[2:3], 0x580
	v_readfirstlane_b32 s0, v145
	v_lshl_add_u64 v[100:101], v[100:101], 0, s[2:3]
	s_mov_b32 m0, s0
	v_readfirstlane_b32 s0, v146
	ds_read_b128 v[110:113], v144
	ds_read_b128 v[114:117], v144 offset:1024
	ds_read_b128 v[138:141], v144 offset:2048
	ds_read_b128 v[148:151], v144 offset:3072
	ds_read_b128 v[152:155], v144 offset:4096
	ds_read_b128 v[156:159], v144 offset:5120
	ds_read_b128 v[160:163], v130
	ds_read_b128 v[164:167], v130 offset:1024
	ds_read_b128 v[174:177], v108
	ds_read_b128 v[178:181], v108 offset:1024
	global_load_lds_dwordx4 v[100:101], off
	v_lshl_add_u64 v[100:101], v[102:103], 0, s[2:3]
	s_mov_b32 m0, s0
	s_nop 0
	global_load_lds_dwordx4 v[100:101], off
	s_barrier
	s_waitcnt lgkmcnt(0)
	s_setprio 1
	s_waitcnt lgkmcnt(0)
	v_mfma_f32_16x16x32_f16 v[94:97], v[160:163], v[110:113], v[94:97]
	v_mfma_f32_16x16x32_f16 v[90:93], v[160:163], v[138:141], v[90:93]
	v_mfma_f32_16x16x32_f16 v[86:89], v[160:163], v[152:155], v[86:89]
	v_mfma_f32_16x16x32_f16 v[74:77], v[174:177], v[110:113], v[74:77]
	v_mfma_f32_16x16x32_f16 v[18:21], v[174:177], v[152:155], v[18:21]
	v_mfma_f32_16x16x32_f16 v[94:97], v[164:167], v[114:117], v[94:97]
	v_mfma_f32_16x16x32_f16 v[90:93], v[164:167], v[148:151], v[90:93]
	v_mfma_f32_16x16x32_f16 v[86:89], v[164:167], v[156:159], v[86:89]
	v_mfma_f32_16x16x32_f16 v[74:77], v[178:181], v[114:117], v[74:77]
	v_mfma_f32_16x16x32_f16 v[46:49], v[174:177], v[138:141], v[46:49]
	v_mfma_f32_16x16x32_f16 v[18:21], v[178:181], v[156:159], v[18:21]
	v_mfma_f32_16x16x32_f16 v[100:103], v[178:181], v[148:151], v[46:49]
	s_setprio 0
	s_barrier
	s_nop 3
	ds_read_b128 v[46:49], v143
	ds_read_b128 v[144:147], v143 offset:1024
	ds_read_b128 v[182:185], v143 offset:2048
	ds_read_b128 v[186:189], v143 offset:3072
	ds_read_b128 v[190:193], v143 offset:4096
	ds_read_b128 v[194:197], v143 offset:5120
	s_barrier
	s_waitcnt lgkmcnt(0)
	s_setprio 1
	s_waitcnt lgkmcnt(0)
	v_mfma_f32_16x16x32_f16 v[34:37], v[174:177], v[182:185], v[34:37]
	v_mfma_f32_16x16x32_f16 v[10:13], v[160:163], v[46:49], v[10:13]
	v_mfma_f32_16x16x32_f16 v[6:9], v[160:163], v[182:185], v[6:9]
	v_mfma_f32_16x16x32_f16 v[2:5], v[160:163], v[190:193], v[2:5]
	v_mfma_f32_16x16x32_f16 v[26:29], v[174:177], v[46:49], v[26:29]
	v_mfma_f32_16x16x32_f16 v[160:163], v[178:181], v[186:189], v[34:37]
	v_mfma_f32_16x16x32_f16 v[34:37], v[174:177], v[190:193], v[50:53]
	v_mfma_f32_16x16x32_f16 v[10:13], v[164:167], v[144:147], v[10:13]
	v_mfma_f32_16x16x32_f16 v[6:9], v[164:167], v[186:189], v[6:9]
	v_mfma_f32_16x16x32_f16 v[2:5], v[164:167], v[194:197], v[2:5]
	v_mfma_f32_16x16x32_f16 v[26:29], v[178:181], v[144:147], v[26:29]
	v_mfma_f32_16x16x32_f16 v[50:53], v[178:181], v[194:197], v[34:37]
	s_setprio 0
	s_barrier
	s_nop 0
	ds_read_b128 v[34:37], v130 offset:16384
	ds_read_b128 v[164:167], v130 offset:17408
	ds_read_b128 v[174:177], v108 offset:16384
	ds_read_b128 v[178:181], v108 offset:17408
	s_waitcnt vmcnt(4)
	s_barrier
	s_waitcnt lgkmcnt(0)
	s_setprio 1
	s_waitcnt lgkmcnt(0)
	v_mfma_f32_16x16x32_f16 v[22:25], v[34:37], v[138:141], v[22:25]
	v_mfma_f32_16x16x32_f16 v[198:201], v[164:167], v[148:151], v[22:25]
	v_mfma_f32_16x16x32_f16 v[22:25], v[34:37], v[152:155], v[30:33]
	v_mfma_f32_16x16x32_f16 v[30:33], v[164:167], v[156:159], v[22:25]
	v_mfma_f32_16x16x32_f16 v[22:25], v[174:177], v[110:113], v[38:41]
	v_mfma_f32_16x16x32_f16 v[14:17], v[34:37], v[110:113], v[14:17]
	v_mfma_f32_16x16x32_f16 v[110:113], v[178:181], v[114:117], v[22:25]
	v_mfma_f32_16x16x32_f16 v[22:25], v[174:177], v[138:141], v[54:57]
	v_mfma_f32_16x16x32_f16 v[14:17], v[164:167], v[114:117], v[14:17]
	v_mfma_f32_16x16x32_f16 v[54:57], v[178:181], v[148:151], v[22:25]
	v_mfma_f32_16x16x32_f16 v[22:25], v[174:177], v[152:155], v[62:65]
	v_mfma_f32_16x16x32_f16 v[114:117], v[178:181], v[156:159], v[22:25]
	s_setprio 0
	s_setprio 1
	v_mfma_f32_16x16x32_f16 v[22:25], v[34:37], v[46:49], v[42:45]
	v_mfma_f32_16x16x32_f16 v[138:141], v[164:167], v[144:147], v[22:25]
	v_mfma_f32_16x16x32_f16 v[22:25], v[34:37], v[182:185], v[58:61]
	v_mfma_f32_16x16x32_f16 v[148:151], v[164:167], v[186:189], v[22:25]
	v_mfma_f32_16x16x32_f16 v[22:25], v[34:37], v[190:193], v[66:69]
	v_mfma_f32_16x16x32_f16 v[152:155], v[164:167], v[194:197], v[22:25]
	v_mfma_f32_16x16x32_f16 v[22:25], v[174:177], v[46:49], v[70:73]
	v_mfma_f32_16x16x32_f16 v[142:145], v[178:181], v[144:147], v[22:25]
	v_mfma_f32_16x16x32_f16 v[22:25], v[174:177], v[182:185], v[78:81]
	v_mfma_f32_16x16x32_f16 v[156:159], v[178:181], v[186:189], v[22:25]
	v_mfma_f32_16x16x32_f16 v[22:25], v[174:177], v[190:193], v[82:85]
	v_mfma_f32_16x16x32_f16 v[164:167], v[178:181], v[194:197], v[22:25]
	s_setprio 0
	s_barrier
	ds_read_b128 v[58:61], v136
	ds_read_b128 v[174:177], v136 offset:1024
	ds_read_b128 v[178:181], v136 offset:2048
	ds_read_b128 v[182:185], v136 offset:3072
	ds_read_b128 v[186:189], v136 offset:4096
	ds_read_b128 v[134:137], v136 offset:5120
	ds_read_b128 v[34:37], v130 offset:32768
	ds_read_b128 v[62:65], v130 offset:33792
	ds_read_b128 v[78:81], v108 offset:32768
	ds_read_b128 v[190:193], v108 offset:33792
	s_waitcnt vmcnt(2)
	s_barrier
	s_waitcnt lgkmcnt(0)
	s_setprio 1
	s_waitcnt lgkmcnt(0)
	v_mfma_f32_16x16x32_f16 v[22:25], v[34:37], v[58:61], v[94:97]
	v_mfma_f32_16x16x32_f16 v[82:85], v[62:65], v[174:177], v[22:25]
	v_mfma_f32_16x16x32_f16 v[22:25], v[34:37], v[178:181], v[90:93]
	v_mfma_f32_16x16x32_f16 v[70:73], v[62:65], v[182:185], v[22:25]
	v_mfma_f32_16x16x32_f16 v[22:25], v[34:37], v[186:189], v[86:89]
	v_mfma_f32_16x16x32_f16 v[46:49], v[62:65], v[134:137], v[22:25]
	v_mfma_f32_16x16x32_f16 v[22:25], v[78:81], v[58:61], v[74:77]
	v_mfma_f32_16x16x32_f16 v[86:89], v[190:193], v[174:177], v[22:25]
	v_mfma_f32_16x16x32_f16 v[22:25], v[78:81], v[178:181], v[100:103]
	v_mfma_f32_16x16x32_f16 v[18:21], v[78:81], v[186:189], v[18:21]
	v_mfma_f32_16x16x32_f16 v[66:69], v[190:193], v[182:185], v[22:25]
	v_mfma_f32_16x16x32_f16 v[42:45], v[190:193], v[134:137], v[18:21]
	s_setprio 0
	s_barrier
	ds_read_b128 v[100:103], v133
	ds_read_b128 v[194:197], v133 offset:1024
	ds_read_b128 v[202:205], v133 offset:2048
	ds_read_b128 v[206:209], v133 offset:3072
	ds_read_b128 v[210:213], v133 offset:4096
	ds_read_b128 v[214:217], v133 offset:5120
	s_waitcnt vmcnt(0)
	s_barrier
	s_waitcnt lgkmcnt(0)
	s_setprio 1
	s_waitcnt lgkmcnt(0)
	v_mfma_f32_16x16x32_f16 v[6:9], v[34:37], v[202:205], v[6:9]
	v_mfma_f32_16x16x32_f16 v[2:5], v[34:37], v[210:213], v[2:5]
	v_mfma_f32_16x16x32_f16 v[22:25], v[62:65], v[206:209], v[6:9]
	v_mfma_f32_16x16x32_f16 v[6:9], v[62:65], v[214:217], v[2:5]
	v_mfma_f32_16x16x32_f16 v[2:5], v[78:81], v[100:103], v[26:29]
	v_mfma_f32_16x16x32_f16 v[10:13], v[34:37], v[100:103], v[10:13]
	v_mfma_f32_16x16x32_f16 v[34:37], v[190:193], v[194:197], v[2:5]
	v_mfma_f32_16x16x32_f16 v[2:5], v[78:81], v[202:205], v[160:163]
	v_mfma_f32_16x16x32_f16 v[18:21], v[190:193], v[206:209], v[2:5]
	v_mfma_f32_16x16x32_f16 v[2:5], v[78:81], v[210:213], v[50:53]
	v_mfma_f32_16x16x32_f16 v[38:41], v[62:65], v[194:197], v[10:13]
	v_mfma_f32_16x16x32_f16 v[2:5], v[190:193], v[214:217], v[2:5]
	s_setprio 0
	s_barrier
	ds_read_b128 v[10:13], v130 offset:49152
	ds_read_b128 v[26:29], v130 offset:50176
	ds_read_b128 v[128:131], v108 offset:49152
	ds_read_b128 v[160:163], v108 offset:50176
	s_barrier
	s_waitcnt lgkmcnt(0)
	s_setprio 1
	s_waitcnt lgkmcnt(0)
	v_mfma_f32_16x16x32_f16 v[14:17], v[10:13], v[58:61], v[14:17]
	v_mfma_f32_16x16x32_f16 v[90:93], v[26:29], v[174:177], v[14:17]
	v_mfma_f32_16x16x32_f16 v[14:17], v[10:13], v[178:181], v[198:201]
	v_mfma_f32_16x16x32_f16 v[78:81], v[26:29], v[182:185], v[14:17]
	v_mfma_f32_16x16x32_f16 v[14:17], v[10:13], v[186:189], v[30:33]
	v_mfma_f32_16x16x32_f16 v[62:65], v[26:29], v[134:137], v[14:17]
	v_mfma_f32_16x16x32_f16 v[14:17], v[128:131], v[58:61], v[110:113]
	v_mfma_f32_16x16x32_f16 v[94:97], v[160:163], v[174:177], v[14:17]
	v_mfma_f32_16x16x32_f16 v[14:17], v[128:131], v[178:181], v[54:57]
	v_mfma_f32_16x16x32_f16 v[74:77], v[160:163], v[182:185], v[14:17]
	v_mfma_f32_16x16x32_f16 v[14:17], v[128:131], v[186:189], v[114:117]
	v_mfma_f32_16x16x32_f16 v[58:61], v[160:163], v[134:137], v[14:17]
	s_setprio 0
	s_setprio 1
	v_mfma_f32_16x16x32_f16 v[14:17], v[10:13], v[100:103], v[138:141]
	v_mfma_f32_16x16x32_f16 v[54:57], v[26:29], v[194:197], v[14:17]
	v_mfma_f32_16x16x32_f16 v[14:17], v[10:13], v[202:205], v[148:151]
	v_mfma_f32_16x16x32_f16 v[10:13], v[10:13], v[210:213], v[152:155]
	v_mfma_f32_16x16x32_f16 v[30:33], v[26:29], v[206:209], v[14:17]
	v_mfma_f32_16x16x32_f16 v[14:17], v[26:29], v[214:217], v[10:13]
	v_mfma_f32_16x16x32_f16 v[10:13], v[128:131], v[100:103], v[142:145]
	v_mfma_f32_16x16x32_f16 v[50:53], v[160:163], v[194:197], v[10:13]
	v_mfma_f32_16x16x32_f16 v[10:13], v[128:131], v[202:205], v[156:159]
	v_mfma_f32_16x16x32_f16 v[26:29], v[160:163], v[206:209], v[10:13]
	v_mfma_f32_16x16x32_f16 v[10:13], v[128:131], v[210:213], v[164:167]
	v_mfma_f32_16x16x32_f16 v[10:13], v[160:163], v[214:217], v[10:13]
	s_setprio 0
	s_movk_i32 s0, 0x100
	v_cmp_gt_u32_e64 s[0:1], s0, v107
	s_barrier
	s_and_saveexec_b64 s[2:3], s[0:1]
	s_cbranch_execz .LBB1_69
	s_barrier

	.amdhsa_kernel _Z11mega_kernelPKfPDF16_PKDF16_S3_S1_PfS0_S0_PK15HIP_vector_typeIfLj2EEPS6_
		.amdhsa_group_segment_fixed_size 0
		.amdhsa_private_segment_fixed_size 0
		.amdhsa_kernarg_size 80
		.amdhsa_user_sgpr_count 2
		.amdhsa_user_sgpr_dispatch_ptr 0
		.amdhsa_user_sgpr_queue_ptr 0
		.amdhsa_user_sgpr_kernarg_segment_ptr 1
		.amdhsa_user_sgpr_dispatch_id 0
		.amdhsa_user_sgpr_kernarg_preload_length 0
		.amdhsa_user_sgpr_kernarg_preload_offset 0
		.amdhsa_user_sgpr_private_segment_size 0
		.amdhsa_uses_dynamic_stack 0
		.amdhsa_enable_private_segment 0
		.amdhsa_system_sgpr_workgroup_id_x 1
		.amdhsa_system_sgpr_workgroup_id_y 0
		.amdhsa_system_sgpr_workgroup_id_z 0
		.amdhsa_system_sgpr_workgroup_info 0
		.amdhsa_system_vgpr_workitem_id 0
		.amdhsa_next_free_vgpr 240
		.amdhsa_next_free_sgpr 102
		.amdhsa_accum_offset 240
		.amdhsa_reserve_vcc 1
		.amdhsa_float_round_mode_32 0
		.amdhsa_float_round_mode_16_64 0
		.amdhsa_float_denorm_mode_32 3
		.amdhsa_float_denorm_mode_16_64 3
		.amdhsa_dx10_clamp 1
		.amdhsa_ieee_mode 1
		.amdhsa_fp16_overflow 0
		.amdhsa_tg_split 0
		.amdhsa_exception_fp_ieee_invalid_op 0
		.amdhsa_exception_fp_denorm_src 0
		.amdhsa_exception_fp_ieee_div_zero 0
		.amdhsa_exception_fp_ieee_overflow 0
		.amdhsa_exception_fp_ieee_underflow 0
		.amdhsa_exception_fp_ieee_inexact 0
		.amdhsa_exception_int_div_zero 0
	.end_amdhsa_kernel

amdhsa.kernels:
  - .agpr_count:     0
    .args:
      - .actual_access:  read_only
        .address_space:  global
        .offset:         0
        .size:           8
        .value_kind:     global_buffer
      - .actual_access:  write_only
        .address_space:  global
        .offset:         8
        .size:           8
        .value_kind:     global_buffer
      - .offset:         16
        .size:           8
        .value_kind:     by_value
      - .actual_access:  read_only
        .address_space:  global
        .offset:         24
        .size:           8
        .value_kind:     global_buffer
      - .actual_access:  read_only
        .address_space:  global
        .offset:         32
        .size:           8
        .value_kind:     global_buffer
      - .actual_access:  read_only
        .address_space:  global
        .offset:         40
        .size:           8
        .value_kind:     global_buffer
      - .actual_access:  read_only
        .address_space:  global
        .offset:         48
        .size:           8
        .value_kind:     global_buffer
      - .actual_access:  read_only
        .address_space:  global
        .offset:         56
        .size:           8
        .value_kind:     global_buffer
      - .actual_access:  write_only
        .address_space:  global
        .offset:         64
        .size:           8
        .value_kind:     global_buffer
      - .actual_access:  write_only
        .address_space:  global
        .offset:         72
        .size:           8
        .value_kind:     global_buffer
      - .actual_access:  write_only
        .address_space:  global
        .offset:         80
        .size:           8
        .value_kind:     global_buffer
      - .actual_access:  write_only
        .address_space:  global
        .offset:         88
        .size:           8
        .value_kind:     global_buffer
      - .actual_access:  write_only
        .address_space:  global
        .offset:         96
        .size:           8
        .value_kind:     global_buffer
      - .actual_access:  write_only
        .address_space:  global
        .offset:         104
        .size:           8
        .value_kind:     global_buffer
    .group_segment_fixed_size: 0
    .kernarg_segment_align: 8
    .kernarg_segment_size: 112
    .language:       OpenCL C
    .language_version:
      - 2
      - 0
    .max_flat_workgroup_size: 256
    .name:           _Z15prep_cvt_kernelPKfPDF16_mS0_S0_S0_S0_S0_S1_S1_P15HIP_vector_typeIfLj2EEPfS4_Py
    .private_segment_fixed_size: 0
    .sgpr_count:     22
    .sgpr_spill_count: 0
    .symbol:         _Z15prep_cvt_kernelPKfPDF16_mS0_S0_S0_S0_S0_S1_S1_P15HIP_vector_typeIfLj2EEPfS4_Py.kd
    .uniform_work_group_size: 1
    .uses_dynamic_stack: false
    .vgpr_count:     25
    .vgpr_spill_count: 0
    .wavefront_size: 64
  - .agpr_count:     0
    .args:
      - .actual_access:  read_only
        .address_space:  global
        .offset:         0
        .size:           8
        .value_kind:     global_buffer
      - .address_space:  global
        .offset:         8
        .size:           8
        .value_kind:     global_buffer
      - .address_space:  global
        .offset:         16
        .size:           8
        .value_kind:     global_buffer
      - .address_space:  global
        .offset:         24
        .size:           8
        .value_kind:     global_buffer
      - .address_space:  global
        .offset:         32
        .size:           8
        .value_kind:     global_buffer
      - .actual_access:  write_only
        .address_space:  global
        .offset:         40
        .size:           8
        .value_kind:     global_buffer
      - .actual_access:  read_only
        .address_space:  global
        .offset:         48
        .size:           8
        .value_kind:     global_buffer
      - .actual_access:  read_only
        .address_space:  global
        .offset:         56
        .size:           8
        .value_kind:     global_buffer
      - .actual_access:  read_only
        .address_space:  global
        .offset:         64
        .size:           8
        .value_kind:     global_buffer
      - .address_space:  global
        .offset:         72
        .size:           8
        .value_kind:     global_buffer
    .group_segment_fixed_size: 0
    .kernarg_segment_align: 8
    .kernarg_segment_size: 80
    .language:       OpenCL C
    .language_version:
      - 2
      - 0
    .max_flat_workgroup_size: 512
    .name:           _Z11mega_kernelPKfPDF16_PKDF16_S3_S1_PfS0_S0_PK15HIP_vector_typeIfLj2EEPS6_
    .private_segment_fixed_size: 0
    .sgpr_count:     108
    .sgpr_spill_count: 15
    .symbol:         _Z11mega_kernelPKfPDF16_PKDF16_S3_S1_PfS0_S0_PK15HIP_vector_typeIfLj2EEPS6_.kd
    .uniform_work_group_size: 1
    .uses_dynamic_stack: false
    .vgpr_count:     240
    .vgpr_spill_count: 0
    .wavefront_size: 64
